# stack10 + pool unit: the vmcnt(0) between the first 20 loads and the remaining 26 removed, single drain at the head of the consumer block (all 46 loads share one round trip)
# baseline (speedup 1.0000x reference)
; #define GAS __attribute__((address_space(1)))
; #define LAS __attribute__((address_space(3)))
; __device__ __forceinline__ unsigned pk2(float lo, float hi) { f32x2_t_ v = {lo, hi}; bf16x2_t_ b = __builtin_convertvector(v, bf16x2_t_); return __builtin_bit_cast(unsigned, b); }
; __device__ __forceinline__ void pool_unit(LAS unsigned char* lds, const bf16* proj, const bf16* poolT, const float* pscale, bf16* Y, int tb, int g, int tid, int lane, int wid, Stopwatch& sw) {
;     ...
;       { v4u pre[15];
; #pragma unroll
;         for (int j = 1; j < 16; ++j) { const v4u z0 = {0u, 0u, 0u, 0u}; pre[j - 1] = (j < win && pos0 - j >= 0) ? *(const GAS v4u*)(up + (long)(tsb * 8 - j) * LDP) : z0; }
; #pragma unroll
;         for (int j = 1; j < 16; ++j) { const v4u w = pre[j - 1];
;           aw[0] += bflo(w.x); aw[1] += bfhi(w.x); aw[2] += bflo(w.y); aw[3] += bfhi(w.y); aw[4] += bflo(w.z); aw[5] += bfhi(w.z); aw[6] += bflo(w.w); aw[7] += bfhi(w.w); } }
;       v4u ww[8], zz[8];
; #pragma unroll
;       for (int tt = 0; tt < 8; ++tt) ww[tt] = *(const GAS v4u*)(up + (long)(tsb * 8 + tt) * LDP);
; #pragma unroll
;       for (int tt = 0; tt < 8; ++tt) { const v4u z0 = {0u, 0u, 0u, 0u}; zz[tt] = (pos0 + tt - (win - 1) >= 0) ? *(const GAS v4u*)(up + (long)(tsb * 8 + tt - (win - 1)) * LDP) : z0; }
; #pragma unroll
;       for (int tt = 0; tt < 8; ++tt) {
;           const int pos = pos0 + tt; const v4u w = ww[tt];
;           float cu[8] = {bflo(w.x), bfhi(w.x), bflo(w.y), bfhi(w.y), bflo(w.z), bfhi(w.z), bflo(w.w), bfhi(w.w)};
; #pragma unroll
;           for (int e = 0; e < 8; ++e) aw[e] += cu[e];
;           const float inv = 1.f / (float)(pos + 1 < win ? pos + 1 : win);
;           v4u o; o.x = pk2(aw[0] * inv - cu[0], aw[1] * inv - cu[1]); o.y = pk2(aw[2] * inv - cu[2], aw[3] * inv - cu[3]); o.z = pk2(aw[4] * inv - cu[4], aw[5] * inv - cu[5]); o.w = pk2(aw[6] * inv - cu[6], aw[7] * inv - cu[7]);
;           *(LAS v4u*)(lds + cc * 2048 + (tsb * 8 + tt) * 16) = o;
;           { const v4u z = zz[tt];
;               aw[0] -= bflo(z.x); aw[1] -= bfhi(z.x); aw[2] -= bflo(z.y); aw[3] -= bfhi(z.y); aw[4] -= bflo(z.z); aw[5] -= bfhi(z.z); aw[6] -= bflo(z.w); aw[7] -= bfhi(z.w); }
.LBB0_278:
	s_or_b64 exec, exec, s[42:43]
	s_waitcnt vmcnt(0)
	v_lshlrev_b32_e32 v196, 16, v43
	v_and_b32_e32 v197, 0xffff0000, v43
	v_pk_add_f32 v[196:197], v[196:197], 0 op_sel_hi:[1,0]
	v_lshlrev_b32_e32 v212, 16, v39
	v_and_b32_e32 v213, 0xffff0000, v39
	v_pk_add_f32 v[196:197], v[196:197], v[212:213]
	v_lshlrev_b32_e32 v212, 16, v55
	v_and_b32_e32 v213, 0xffff0000, v55
	v_pk_add_f32 v[196:197], v[196:197], v[212:213]
	v_lshlrev_b32_e32 v212, 16, v51
	v_and_b32_e32 v213, 0xffff0000, v51
	v_pk_add_f32 v[196:197], v[196:197], v[212:213]
	v_lshlrev_b32_e32 v212, 16, v135
	v_and_b32_e32 v213, 0xffff0000, v135
	v_pk_add_f32 v[196:197], v[196:197], v[212:213]
	v_lshlrev_b32_e32 v212, 16, v131
	v_and_b32_e32 v213, 0xffff0000, v131
	v_pk_add_f32 v[196:197], v[196:197], v[212:213]
	v_lshlrev_b32_e32 v212, 16, v163
	v_and_b32_e32 v213, 0xffff0000, v163
	v_pk_add_f32 v[196:197], v[196:197], v[212:213]
	v_lshlrev_b32_e32 v212, 16, v42
	v_and_b32_e32 v213, 0xffff0000, v42
	v_pk_add_f32 v[212:213], v[212:213], 0 op_sel_hi:[1,0]
	v_lshlrev_b32_e32 v214, 16, v38
	v_and_b32_e32 v215, 0xffff0000, v38
	v_pk_add_f32 v[38:39], v[212:213], v[214:215]
	v_lshlrev_b32_e32 v212, 16, v54
	v_and_b32_e32 v213, 0xffff0000, v54
	v_pk_add_f32 v[38:39], v[38:39], v[212:213]
	v_lshlrev_b32_e32 v212, 16, v50
	v_and_b32_e32 v213, 0xffff0000, v50
	v_pk_add_f32 v[38:39], v[38:39], v[212:213]
	v_lshlrev_b32_e32 v212, 16, v134
	v_and_b32_e32 v213, 0xffff0000, v134
	v_pk_add_f32 v[38:39], v[38:39], v[212:213]
	v_lshlrev_b32_e32 v134, 16, v130
	v_and_b32_e32 v135, 0xffff0000, v130
	v_pk_add_f32 v[38:39], v[38:39], v[134:135]
	v_lshlrev_b32_e32 v130, 16, v162
	v_and_b32_e32 v131, 0xffff0000, v162
	v_pk_add_f32 v[130:131], v[38:39], v[130:131]
	v_lshlrev_b32_e32 v38, 16, v41
	v_and_b32_e32 v39, 0xffff0000, v41
	v_and_b32_e32 v191, 0xffff0000, v175
	v_lshlrev_b32_e32 v190, 16, v175
	v_and_b32_e32 v55, 0xffff0000, v174
	v_lshlrev_b32_e32 v54, 16, v174
	v_pk_add_f32 v[38:39], v[38:39], 0 op_sel_hi:[1,0]
	v_lshlrev_b32_e32 v174, 16, v37
	v_and_b32_e32 v175, 0xffff0000, v37
	v_pk_add_f32 v[38:39], v[38:39], v[174:175]
	v_lshlrev_b32_e32 v174, 16, v53
	v_and_b32_e32 v175, 0xffff0000, v53
	v_and_b32_e32 v193, 0xffff0000, v179
	v_lshlrev_b32_e32 v192, 16, v179
	v_and_b32_e32 v51, 0xffff0000, v178
	v_lshlrev_b32_e32 v50, 16, v178
	v_pk_add_f32 v[38:39], v[38:39], v[174:175]
	v_lshlrev_b32_e32 v174, 16, v49
	v_and_b32_e32 v175, 0xffff0000, v49
	v_lshlrev_b32_e32 v178, 16, v40
	v_and_b32_e32 v179, 0xffff0000, v40
	v_pk_add_f32 v[38:39], v[38:39], v[174:175]
	v_lshlrev_b32_e32 v174, 16, v133
	v_and_b32_e32 v175, 0xffff0000, v133
	v_pk_add_f32 v[178:179], v[178:179], 0 op_sel_hi:[1,0]
	v_lshlrev_b32_e32 v212, 16, v36
	v_and_b32_e32 v213, 0xffff0000, v36
	v_pk_add_f32 v[38:39], v[38:39], v[174:175]
	v_lshlrev_b32_e32 v174, 16, v129
	v_and_b32_e32 v175, 0xffff0000, v129
	v_pk_add_f32 v[36:37], v[178:179], v[212:213]
	v_lshlrev_b32_e32 v178, 16, v52
	v_and_b32_e32 v179, 0xffff0000, v52
	v_pk_add_f32 v[38:39], v[38:39], v[174:175]
	v_lshlrev_b32_e32 v174, 16, v161
	v_and_b32_e32 v175, 0xffff0000, v161
	v_pk_add_f32 v[36:37], v[36:37], v[178:179]
	v_lshlrev_b32_e32 v52, 16, v48
	v_and_b32_e32 v53, 0xffff0000, v48
	v_pk_add_f32 v[174:175], v[38:39], v[174:175]
	v_pk_add_f32 v[36:37], v[36:37], v[52:53]
	v_lshlrev_b32_e32 v52, 16, v132
	v_and_b32_e32 v53, 0xffff0000, v132
	v_min_i32_e32 v38, s0, v211
	v_pk_add_f32 v[36:37], v[36:37], v[52:53]
	v_lshlrev_b32_e32 v52, 16, v128
	v_and_b32_e32 v53, 0xffff0000, v128
	v_cvt_f32_i32_e32 v128, v38
	v_pk_add_f32 v[36:37], v[36:37], v[52:53]
	v_lshlrev_b32_e32 v52, 16, v160
	v_and_b32_e32 v53, 0xffff0000, v160
	v_pk_add_f32 v[52:53], v[36:37], v[52:53]
	v_div_scale_f32 v37, s[18:19], v128, v128, 1.0
	v_rcp_f32_e32 v129, v37
	v_and_b32_e32 v39, 0xffff0000, v148
	v_lshlrev_b32_e32 v38, 16, v148
	v_and_b32_e32 v41, 0xffff0000, v176
	v_lshlrev_b32_e32 v40, 16, v176
	v_pk_add_f32 v[38:39], v[52:53], v[38:39]
	v_and_b32_e32 v49, 0xffff0000, v172
	v_lshlrev_b32_e32 v48, 16, v172
	v_fma_f32 v132, -v37, v129, 1.0
	v_pk_add_f32 v[38:39], v[38:39], v[40:41]
	v_fmac_f32_e32 v129, v132, v129
	v_div_scale_f32 v132, vcc, 1.0, v128, 1.0
	v_pk_add_f32 v[38:39], v[38:39], v[48:49]
	v_lshlrev_b32_e32 v40, 16, v140
	v_and_b32_e32 v41, 0xffff0000, v140
	v_mul_f32_e32 v133, v132, v129
	v_pk_add_f32 v[38:39], v[38:39], v[40:41]
	v_lshlrev_b32_e32 v40, 16, v136
	v_and_b32_e32 v41, 0xffff0000, v136
	v_fma_f32 v148, -v37, v133, v132
	v_pk_add_f32 v[38:39], v[38:39], v[40:41]
	v_lshlrev_b32_e32 v40, 16, v168
	v_and_b32_e32 v41, 0xffff0000, v168
	v_fmac_f32_e32 v133, v148, v129
	v_pk_add_f32 v[38:39], v[38:39], v[40:41]
	v_lshlrev_b32_e32 v40, 16, v164
	v_and_b32_e32 v41, 0xffff0000, v164
	v_fma_f32 v37, -v37, v133, v132
	v_pk_add_f32 v[38:39], v[38:39], v[40:41]
	v_lshlrev_b32_e32 v40, 16, v180
	v_and_b32_e32 v41, 0xffff0000, v180
	v_div_fmas_f32 v37, v37, v129, v133
	v_pk_add_f32 v[38:39], v[38:39], v[40:41]
	v_lshlrev_b32_e32 v40, 16, v184
	v_and_b32_e32 v41, 0xffff0000, v184
	v_and_b32_e32 v135, 0xffff0000, v149
	v_lshlrev_b32_e32 v134, 16, v149
	v_div_fixup_f32 v128, v37, v128, 1.0
	v_pk_add_f32 v[48:49], v[38:39], v[40:41]
	v_and_b32_e32 v195, 0xffff0000, v151
	v_lshlrev_b32_e32 v194, 16, v151
	v_and_b32_e32 v43, 0xffff0000, v150
	v_lshlrev_b32_e32 v42, 16, v150
	v_and_b32_e32 v151, 0xffff0000, v177
	v_lshlrev_b32_e32 v150, 16, v177
	v_pk_fma_f32 v[38:39], v[128:129], v[48:49], v[40:41] op_sel_hi:[0,1,1] neg_lo:[0,0,1] neg_hi:[0,0,1]
	v_pk_add_f32 v[40:41], v[174:175], v[134:135]
	v_and_b32_e32 v163, 0xffff0000, v173
	v_lshlrev_b32_e32 v162, 16, v173
	v_pk_add_f32 v[40:41], v[40:41], v[150:151]
; #define LAS __attribute__((address_space(3)))
; __device__ __forceinline__ unsigned pk2(float lo, float hi) { f32x2_t_ v = {lo, hi}; bf16x2_t_ b = __builtin_convertvector(v, bf16x2_t_); return __builtin_bit_cast(unsigned, b); }
; __device__ __forceinline__ void pool_unit(LAS unsigned char* lds, const bf16* proj, const bf16* poolT, const float* pscale, bf16* Y, int tb, int g, int tid, int lane, int wid, Stopwatch& sw) {
;     ...
;       for (int tt = 0; tt < 8; ++tt) {
;           const int pos = pos0 + tt; const v4u w = ww[tt];
;           float cu[8] = {bflo(w.x), bfhi(w.x), bflo(w.y), bfhi(w.y), bflo(w.z), bfhi(w.z), bflo(w.w), bfhi(w.w)};
; #pragma unroll
;           for (int e = 0; e < 8; ++e) aw[e] += cu[e];
;           const float inv = 1.f / (float)(pos + 1 < win ? pos + 1 : win);
;           v4u o; o.x = pk2(aw[0] * inv - cu[0], aw[1] * inv - cu[1]); o.y = pk2(aw[2] * inv - cu[2], aw[3] * inv - cu[3]); o.z = pk2(aw[4] * inv - cu[4], aw[5] * inv - cu[5]); o.w = pk2(aw[6] * inv - cu[6], aw[7] * inv - cu[7]);
;           *(LAS v4u*)(lds + cc * 2048 + (tsb * 8 + tt) * 16) = o;
;           { const v4u z = zz[tt];
;               aw[0] -= bflo(z.x); aw[1] -= bfhi(z.x); aw[2] -= bflo(z.y); aw[3] -= bfhi(z.y); aw[4] -= bflo(z.z); aw[5] -= bfhi(z.z); aw[6] -= bflo(z.w); aw[7] -= bfhi(z.w); }
	v_lshlrev_b32_e32 v52, 16, v141
	v_pk_add_f32 v[40:41], v[40:41], v[162:163]
	v_and_b32_e32 v53, 0xffff0000, v141
	v_pk_add_f32 v[40:41], v[40:41], v[52:53]
	v_lshlrev_b32_e32 v52, 16, v137
	v_and_b32_e32 v53, 0xffff0000, v137
	v_pk_add_f32 v[40:41], v[40:41], v[52:53]
	v_lshlrev_b32_e32 v52, 16, v169
	v_and_b32_e32 v53, 0xffff0000, v169
	v_pk_add_f32 v[40:41], v[40:41], v[52:53]
	v_lshlrev_b32_e32 v52, 16, v165
	v_and_b32_e32 v53, 0xffff0000, v165
	v_pk_add_f32 v[40:41], v[40:41], v[52:53]
	v_lshlrev_b32_e32 v52, 16, v181
	v_and_b32_e32 v53, 0xffff0000, v181
	v_pk_add_f32 v[40:41], v[40:41], v[52:53]
	v_lshlrev_b32_e32 v52, 16, v185
	v_and_b32_e32 v53, 0xffff0000, v185
	v_pk_add_f32 v[132:133], v[40:41], v[52:53]
	v_cvt_pk_bf16_f32 v38, v38, v39
	v_pk_fma_f32 v[40:41], v[128:129], v[132:133], v[52:53] op_sel_hi:[0,1,1] neg_lo:[0,0,1] neg_hi:[0,0,1]
	v_cvt_pk_bf16_f32 v39, v40, v41
	v_pk_add_f32 v[40:41], v[130:131], v[42:43]
	v_lshlrev_b32_e32 v42, 16, v142
	v_pk_add_f32 v[40:41], v[40:41], v[50:51]
	v_and_b32_e32 v43, 0xffff0000, v142
	v_pk_add_f32 v[40:41], v[40:41], v[54:55]
	v_min_i32_e32 v37, s0, v210
	v_pk_add_f32 v[40:41], v[40:41], v[42:43]
	v_lshlrev_b32_e32 v42, 16, v138
	v_and_b32_e32 v43, 0xffff0000, v138
	v_pk_add_f32 v[40:41], v[40:41], v[42:43]
	v_lshlrev_b32_e32 v42, 16, v170
	v_and_b32_e32 v43, 0xffff0000, v170
	v_pk_add_f32 v[40:41], v[40:41], v[42:43]
	v_lshlrev_b32_e32 v42, 16, v166
	v_and_b32_e32 v43, 0xffff0000, v166
	v_pk_add_f32 v[40:41], v[40:41], v[42:43]
	v_lshlrev_b32_e32 v42, 16, v182
	v_and_b32_e32 v43, 0xffff0000, v182
	v_pk_add_f32 v[40:41], v[40:41], v[42:43]
	v_lshlrev_b32_e32 v42, 16, v186
	v_and_b32_e32 v43, 0xffff0000, v186
	v_pk_add_f32 v[50:51], v[40:41], v[42:43]
	v_lshlrev_b32_e32 v52, 16, v143
	v_pk_fma_f32 v[40:41], v[128:129], v[50:51], v[42:43] op_sel_hi:[0,1,1] neg_lo:[0,0,1] neg_hi:[0,0,1]
	v_pk_add_f32 v[42:43], v[196:197], v[194:195]
	v_and_b32_e32 v53, 0xffff0000, v143
	v_pk_add_f32 v[42:43], v[42:43], v[192:193]
	v_cvt_f32_i32_e32 v37, v37
	v_pk_add_f32 v[42:43], v[42:43], v[190:191]
	v_lshl_add_u32 v36, v205, 11, 0
	v_pk_add_f32 v[42:43], v[42:43], v[52:53]
	v_lshlrev_b32_e32 v52, 16, v139
	v_and_b32_e32 v53, 0xffff0000, v139
	v_pk_add_f32 v[42:43], v[42:43], v[52:53]
	v_lshlrev_b32_e32 v52, 16, v171
	v_and_b32_e32 v53, 0xffff0000, v171
	v_pk_add_f32 v[42:43], v[42:43], v[52:53]
	v_lshlrev_b32_e32 v52, 16, v167
	v_and_b32_e32 v53, 0xffff0000, v167
	v_pk_add_f32 v[42:43], v[42:43], v[52:53]
	v_lshlrev_b32_e32 v52, 16, v183
	v_and_b32_e32 v53, 0xffff0000, v183
	v_div_scale_f32 v54, s[18:19], v37, v37, 1.0
	v_pk_add_f32 v[42:43], v[42:43], v[52:53]
	v_lshlrev_b32_e32 v52, 16, v187
	v_and_b32_e32 v53, 0xffff0000, v187
	v_rcp_f32_e32 v55, v54
	v_pk_add_f32 v[42:43], v[42:43], v[52:53]
	v_cvt_pk_bf16_f32 v40, v40, v41
	v_pk_fma_f32 v[52:53], v[128:129], v[42:43], v[52:53] op_sel_hi:[0,1,1] neg_lo:[0,0,1] neg_hi:[0,0,1]
	v_cvt_pk_bf16_f32 v41, v52, v53
	v_lshl_add_u32 v130, v204, 4, v36
	ds_write_b128 v130, v[38:41]
	v_fma_f32 v38, -v54, v55, 1.0
	v_fmac_f32_e32 v55, v38, v55
	v_div_scale_f32 v38, vcc, 1.0, v37, 1.0
	v_mul_f32_e32 v39, v38, v55
	v_fma_f32 v40, -v54, v39, v38
	v_fmac_f32_e32 v39, v40, v55
	v_fma_f32 v38, -v54, v39, v38
	v_div_fmas_f32 v38, v38, v55, v39
	v_div_fixup_f32 v52, v38, v37, 1.0
	v_lshlrev_b32_e32 v38, 16, v144
	v_and_b32_e32 v39, 0xffff0000, v144
	v_pk_add_f32 v[38:39], v[48:49], v[38:39] neg_lo:[0,1] neg_hi:[0,1]
	v_lshlrev_b32_e32 v40, 16, v152
	v_and_b32_e32 v41, 0xffff0000, v152
	v_pk_add_f32 v[48:49], v[38:39], v[40:41]
	v_lshlrev_b32_e32 v54, 16, v153
	v_pk_fma_f32 v[38:39], v[52:53], v[48:49], v[40:41] op_sel_hi:[0,1,1] neg_lo:[0,0,1] neg_hi:[0,0,1]
	v_lshlrev_b32_e32 v40, 16, v145
	v_and_b32_e32 v41, 0xffff0000, v145
	v_pk_add_f32 v[40:41], v[132:133], v[40:41] neg_lo:[0,1] neg_hi:[0,1]
	v_and_b32_e32 v55, 0xffff0000, v153
	v_pk_add_f32 v[128:129], v[40:41], v[54:55]
	v_min_i32_e32 v37, s0, v209
	v_pk_fma_f32 v[40:41], v[52:53], v[128:129], v[54:55] op_sel_hi:[0,1,1] neg_lo:[0,0,1] neg_hi:[0,0,1]
	v_cvt_f32_i32_e32 v37, v37
	v_cvt_pk_bf16_f32 v38, v38, v39
	v_cvt_pk_bf16_f32 v39, v40, v41
	v_lshlrev_b32_e32 v40, 16, v146
	v_and_b32_e32 v41, 0xffff0000, v146
	v_pk_add_f32 v[40:41], v[50:51], v[40:41] neg_lo:[0,1] neg_hi:[0,1]
	v_lshlrev_b32_e32 v50, 16, v154
	v_and_b32_e32 v51, 0xffff0000, v154
	v_pk_add_f32 v[54:55], v[40:41], v[50:51]
	s_xor_b64 s[42:43], s[40:41], -1
	v_pk_fma_f32 v[40:41], v[52:53], v[54:55], v[50:51] op_sel_hi:[0,1,1] neg_lo:[0,0,1] neg_hi:[0,0,1]
	v_lshlrev_b32_e32 v50, 16, v147
	v_and_b32_e32 v51, 0xffff0000, v147
	v_div_scale_f32 v53, s[18:19], v37, v37, 1.0
	v_pk_add_f32 v[42:43], v[42:43], v[50:51] neg_lo:[0,1] neg_hi:[0,1]
	v_lshlrev_b32_e32 v50, 16, v155
	v_and_b32_e32 v51, 0xffff0000, v155
	v_rcp_f32_e32 v131, v53
	v_pk_add_f32 v[42:43], v[42:43], v[50:51]
	v_cvt_pk_bf16_f32 v40, v40, v41
	v_pk_fma_f32 v[50:51], v[52:53], v[42:43], v[50:51] op_sel_hi:[0,1,1] neg_lo:[0,0,1] neg_hi:[0,0,1]
	v_cvt_pk_bf16_f32 v41, v50, v51
	ds_write_b128 v130, v[38:41] offset:16
	v_fma_f32 v38, -v53, v131, 1.0
	v_fmac_f32_e32 v131, v38, v131
	v_div_scale_f32 v38, vcc, 1.0, v37, 1.0
	v_mul_f32_e32 v39, v38, v131
	v_fma_f32 v40, -v53, v39, v38
	v_fmac_f32_e32 v39, v40, v131
	v_fma_f32 v38, -v53, v39, v38
	v_div_fmas_f32 v38, v38, v131, v39
	v_div_fixup_f32 v50, v38, v37, 1.0
	v_lshlrev_b32_e32 v38, 16, v156
	v_and_b32_e32 v39, 0xffff0000, v156
	v_pk_add_f32 v[38:39], v[48:49], v[38:39] neg_lo:[0,1] neg_hi:[0,1]
	v_lshlrev_b32_e32 v40, 16, v64
	v_and_b32_e32 v41, 0xffff0000, v64
	v_pk_add_f32 v[48:49], v[38:39], v[40:41]
	v_lshlrev_b32_e32 v52, 16, v65
; #define LAS __attribute__((address_space(3)))
; __device__ __forceinline__ unsigned pk2(float lo, float hi) { f32x2_t_ v = {lo, hi}; bf16x2_t_ b = __builtin_convertvector(v, bf16x2_t_); return __builtin_bit_cast(unsigned, b); }
; __device__ __forceinline__ void pool_unit(LAS unsigned char* lds, const bf16* proj, const bf16* poolT, const float* pscale, bf16* Y, int tb, int g, int tid, int lane, int wid, Stopwatch& sw) {
;     ...
;       for (int tt = 0; tt < 8; ++tt) {
;           const int pos = pos0 + tt; const v4u w = ww[tt];
;           float cu[8] = {bflo(w.x), bfhi(w.x), bflo(w.y), bfhi(w.y), bflo(w.z), bfhi(w.z), bflo(w.w), bfhi(w.w)};
; #pragma unroll
;           for (int e = 0; e < 8; ++e) aw[e] += cu[e];
;           const float inv = 1.f / (float)(pos + 1 < win ? pos + 1 : win);
;           v4u o; o.x = pk2(aw[0] * inv - cu[0], aw[1] * inv - cu[1]); o.y = pk2(aw[2] * inv - cu[2], aw[3] * inv - cu[3]); o.z = pk2(aw[4] * inv - cu[4], aw[5] * inv - cu[5]); o.w = pk2(aw[6] * inv - cu[6], aw[7] * inv - cu[7]);
;           *(LAS v4u*)(lds + cc * 2048 + (tsb * 8 + tt) * 16) = o;
;           { const v4u z = zz[tt];
;               aw[0] -= bflo(z.x); aw[1] -= bfhi(z.x); aw[2] -= bflo(z.y); aw[3] -= bfhi(z.y); aw[4] -= bflo(z.z); aw[5] -= bfhi(z.z); aw[6] -= bflo(z.w); aw[7] -= bfhi(z.w); }
	v_pk_fma_f32 v[38:39], v[50:51], v[48:49], v[40:41] op_sel_hi:[0,1,1] neg_lo:[0,0,1] neg_hi:[0,0,1]
	v_lshlrev_b32_e32 v40, 16, v157
	v_and_b32_e32 v41, 0xffff0000, v157
	v_pk_add_f32 v[40:41], v[128:129], v[40:41] neg_lo:[0,1] neg_hi:[0,1]
	v_and_b32_e32 v53, 0xffff0000, v65
	v_pk_add_f32 v[64:65], v[40:41], v[52:53]
	v_min_i32_e32 v37, s0, v208
	v_pk_fma_f32 v[40:41], v[50:51], v[64:65], v[52:53] op_sel_hi:[0,1,1] neg_lo:[0,0,1] neg_hi:[0,0,1]
	v_cvt_f32_i32_e32 v37, v37
	v_cvt_pk_bf16_f32 v38, v38, v39
	v_cvt_pk_bf16_f32 v39, v40, v41
	v_lshlrev_b32_e32 v40, 16, v158
	v_and_b32_e32 v41, 0xffff0000, v158
	v_pk_add_f32 v[40:41], v[54:55], v[40:41] neg_lo:[0,1] neg_hi:[0,1]
	v_lshlrev_b32_e32 v52, 16, v66
	v_and_b32_e32 v53, 0xffff0000, v66
	v_pk_add_f32 v[54:55], v[40:41], v[52:53]
	v_div_scale_f32 v66, s[18:19], v37, v37, 1.0
	v_pk_fma_f32 v[40:41], v[50:51], v[54:55], v[52:53] op_sel_hi:[0,1,1] neg_lo:[0,0,1] neg_hi:[0,0,1]
	v_lshlrev_b32_e32 v52, 16, v159
	v_and_b32_e32 v53, 0xffff0000, v159
	v_pk_add_f32 v[42:43], v[42:43], v[52:53] neg_lo:[0,1] neg_hi:[0,1]
	v_lshlrev_b32_e32 v52, 16, v67
	v_and_b32_e32 v53, 0xffff0000, v67
	v_rcp_f32_e32 v67, v66
	v_pk_add_f32 v[42:43], v[42:43], v[52:53]
	v_cvt_pk_bf16_f32 v40, v40, v41
	v_pk_fma_f32 v[50:51], v[50:51], v[42:43], v[52:53] op_sel_hi:[0,1,1] neg_lo:[0,0,1] neg_hi:[0,0,1]
	v_cvt_pk_bf16_f32 v41, v50, v51
	ds_write_b128 v130, v[38:41] offset:32
	v_fma_f32 v38, -v66, v67, 1.0
	v_fmac_f32_e32 v67, v38, v67
	v_div_scale_f32 v38, vcc, 1.0, v37, 1.0
	v_mul_f32_e32 v39, v38, v67
	v_fma_f32 v40, -v66, v39, v38
	v_fmac_f32_e32 v39, v40, v67
	v_fma_f32 v38, -v66, v39, v38
	v_div_fmas_f32 v38, v38, v67, v39
	v_div_fixup_f32 v50, v38, v37, 1.0
	v_lshlrev_b32_e32 v38, 16, v60
	v_and_b32_e32 v39, 0xffff0000, v60
	v_pk_add_f32 v[38:39], v[48:49], v[38:39] neg_lo:[0,1] neg_hi:[0,1]
	v_lshlrev_b32_e32 v40, 16, v44
	v_and_b32_e32 v41, 0xffff0000, v44
	v_pk_add_f32 v[48:49], v[38:39], v[40:41]
	v_lshlrev_b32_e32 v44, 16, v45
	v_pk_fma_f32 v[38:39], v[50:51], v[48:49], v[40:41] op_sel_hi:[0,1,1] neg_lo:[0,0,1] neg_hi:[0,0,1]
	v_lshlrev_b32_e32 v40, 16, v61
	v_and_b32_e32 v41, 0xffff0000, v61
	v_pk_add_f32 v[40:41], v[64:65], v[40:41] neg_lo:[0,1] neg_hi:[0,1]
	v_and_b32_e32 v45, 0xffff0000, v45
	v_pk_add_f32 v[52:53], v[40:41], v[44:45]
	v_min_i32_e32 v37, s0, v207
	v_pk_fma_f32 v[40:41], v[50:51], v[52:53], v[44:45] op_sel_hi:[0,1,1] neg_lo:[0,0,1] neg_hi:[0,0,1]
	v_cvt_f32_i32_e32 v37, v37
	v_cvt_pk_bf16_f32 v38, v38, v39
	v_cvt_pk_bf16_f32 v39, v40, v41
	v_lshlrev_b32_e32 v40, 16, v62
	v_and_b32_e32 v41, 0xffff0000, v62
	v_pk_add_f32 v[40:41], v[54:55], v[40:41] neg_lo:[0,1] neg_hi:[0,1]
	v_lshlrev_b32_e32 v44, 16, v46
	v_and_b32_e32 v45, 0xffff0000, v46
	v_pk_add_f32 v[54:55], v[40:41], v[44:45]
	v_div_scale_f32 v46, s[18:19], v37, v37, 1.0
	v_pk_fma_f32 v[40:41], v[50:51], v[54:55], v[44:45] op_sel_hi:[0,1,1] neg_lo:[0,0,1] neg_hi:[0,0,1]
	v_lshlrev_b32_e32 v44, 16, v63
	v_and_b32_e32 v45, 0xffff0000, v63
	v_pk_add_f32 v[42:43], v[42:43], v[44:45] neg_lo:[0,1] neg_hi:[0,1]
	v_lshlrev_b32_e32 v44, 16, v47
	v_and_b32_e32 v45, 0xffff0000, v47
	v_rcp_f32_e32 v47, v46
	v_pk_add_f32 v[42:43], v[42:43], v[44:45]
	v_cvt_pk_bf16_f32 v40, v40, v41
	v_pk_fma_f32 v[44:45], v[50:51], v[42:43], v[44:45] op_sel_hi:[0,1,1] neg_lo:[0,0,1] neg_hi:[0,0,1]
	v_cvt_pk_bf16_f32 v41, v44, v45
	ds_write_b128 v130, v[38:41] offset:48
	v_fma_f32 v38, -v46, v47, 1.0
	v_fmac_f32_e32 v47, v38, v47
	v_div_scale_f32 v38, vcc, 1.0, v37, 1.0
	v_mul_f32_e32 v39, v38, v47
	v_fma_f32 v40, -v46, v39, v38
	v_fmac_f32_e32 v39, v40, v47
	v_fma_f32 v38, -v46, v39, v38
	v_lshlrev_b32_e32 v40, 16, v56
	v_and_b32_e32 v41, 0xffff0000, v56
	v_div_fmas_f32 v38, v38, v47, v39
	v_pk_add_f32 v[40:41], v[48:49], v[40:41] neg_lo:[0,1] neg_hi:[0,1]
	v_lshlrev_b32_e32 v44, 16, v24
	v_and_b32_e32 v45, 0xffff0000, v24
	v_div_fixup_f32 v38, v38, v37, 1.0
	v_pk_add_f32 v[40:41], v[40:41], v[44:45]
	v_lshlrev_b32_e32 v46, 16, v25
	v_pk_fma_f32 v[44:45], v[38:39], v[40:41], v[44:45] op_sel_hi:[0,1,1] neg_lo:[0,0,1] neg_hi:[0,0,1]
	v_cvt_pk_bf16_f32 v24, v44, v45
	v_lshlrev_b32_e32 v44, 16, v57
	v_and_b32_e32 v45, 0xffff0000, v57
	v_pk_add_f32 v[44:45], v[52:53], v[44:45] neg_lo:[0,1] neg_hi:[0,1]
	v_and_b32_e32 v47, 0xffff0000, v25
	v_pk_add_f32 v[44:45], v[44:45], v[46:47]
	v_min_i32_e32 v37, s0, v206
	v_pk_fma_f32 v[46:47], v[38:39], v[44:45], v[46:47] op_sel_hi:[0,1,1] neg_lo:[0,0,1] neg_hi:[0,0,1]
	v_cvt_pk_bf16_f32 v25, v46, v47
	v_lshlrev_b32_e32 v46, 16, v58
	v_and_b32_e32 v47, 0xffff0000, v58
	v_cvt_f32_i32_e32 v37, v37
	v_pk_add_f32 v[46:47], v[54:55], v[46:47] neg_lo:[0,1] neg_hi:[0,1]
	v_lshlrev_b32_e32 v48, 16, v26
	v_and_b32_e32 v49, 0xffff0000, v26
	v_pk_add_f32 v[46:47], v[46:47], v[48:49]
	v_div_scale_f32 v50, s[18:19], v37, v37, 1.0
	v_pk_fma_f32 v[48:49], v[38:39], v[46:47], v[48:49] op_sel_hi:[0,1,1] neg_lo:[0,0,1] neg_hi:[0,0,1]
	v_cvt_pk_bf16_f32 v26, v48, v49
	v_lshlrev_b32_e32 v48, 16, v59
	v_and_b32_e32 v49, 0xffff0000, v59
	v_pk_add_f32 v[42:43], v[42:43], v[48:49] neg_lo:[0,1] neg_hi:[0,1]
	v_lshlrev_b32_e32 v48, 16, v27
	v_and_b32_e32 v49, 0xffff0000, v27
	v_rcp_f32_e32 v51, v50
	v_pk_add_f32 v[42:43], v[42:43], v[48:49]
	s_nop 0
	v_pk_fma_f32 v[38:39], v[38:39], v[42:43], v[48:49] op_sel_hi:[0,1,1] neg_lo:[0,0,1] neg_hi:[0,0,1]
	v_cvt_pk_bf16_f32 v27, v38, v39
	ds_write_b128 v130, v[24:27] offset:64
	v_fma_f32 v24, -v50, v51, 1.0
	v_fmac_f32_e32 v51, v24, v51
	v_div_scale_f32 v24, vcc, 1.0, v37, 1.0
	v_mul_f32_e32 v25, v24, v51
	v_fma_f32 v26, -v50, v25, v24
	v_fmac_f32_e32 v25, v26, v51
	v_fma_f32 v24, -v50, v25, v24
; #define LAS __attribute__((address_space(3)))
; #define WG_BAR() do { asm volatile("s_waitcnt vmcnt(0) lgkmcnt(0)" ::: "memory"); __builtin_amdgcn_s_barrier(); asm volatile("" ::: "memory"); } while (0)
; __device__ __forceinline__ unsigned pk2(float lo, float hi) { f32x2_t_ v = {lo, hi}; bf16x2_t_ b = __builtin_convertvector(v, bf16x2_t_); return __builtin_bit_cast(unsigned, b); }
; __device__ __forceinline__ void pool_unit(LAS unsigned char* lds, const bf16* proj, const bf16* poolT, const float* pscale, bf16* Y, int tb, int g, int tid, int lane, int wid, Stopwatch& sw) {
;     ...
;       for (int tt = 0; tt < 8; ++tt) {
;           const int pos = pos0 + tt; const v4u w = ww[tt];
;           float cu[8] = {bflo(w.x), bfhi(w.x), bflo(w.y), bfhi(w.y), bflo(w.z), bfhi(w.z), bflo(w.w), bfhi(w.w)};
; #pragma unroll
;           for (int e = 0; e < 8; ++e) aw[e] += cu[e];
;           const float inv = 1.f / (float)(pos + 1 < win ? pos + 1 : win);
;           v4u o; o.x = pk2(aw[0] * inv - cu[0], aw[1] * inv - cu[1]); o.y = pk2(aw[2] * inv - cu[2], aw[3] * inv - cu[3]); o.z = pk2(aw[4] * inv - cu[4], aw[5] * inv - cu[5]); o.w = pk2(aw[6] * inv - cu[6], aw[7] * inv - cu[7]);
;           *(LAS v4u*)(lds + cc * 2048 + (tsb * 8 + tt) * 16) = o;
;           { const v4u z = zz[tt];
;               aw[0] -= bflo(z.x); aw[1] -= bfhi(z.x); aw[2] -= bflo(z.y); aw[3] -= bfhi(z.y); aw[4] -= bflo(z.z); aw[5] -= bfhi(z.z); aw[6] -= bflo(z.w); aw[7] -= bfhi(z.w); }
;       } }
;     WG_BAR();
	v_lshlrev_b32_e32 v26, 16, v32
	v_and_b32_e32 v27, 0xffff0000, v32
	v_div_fmas_f32 v24, v24, v51, v25
	v_pk_add_f32 v[26:27], v[40:41], v[26:27] neg_lo:[0,1] neg_hi:[0,1]
	v_lshlrev_b32_e32 v38, 16, v16
	v_and_b32_e32 v39, 0xffff0000, v16
	v_div_fixup_f32 v24, v24, v37, 1.0
	v_pk_add_f32 v[26:27], v[26:27], v[38:39]
	v_lshlrev_b32_e32 v32, 16, v33
	v_pk_fma_f32 v[38:39], v[24:25], v[26:27], v[38:39] op_sel_hi:[0,1,1] neg_lo:[0,0,1] neg_hi:[0,0,1]
	v_and_b32_e32 v33, 0xffff0000, v33
	v_cvt_pk_bf16_f32 v16, v38, v39
	v_pk_add_f32 v[32:33], v[44:45], v[32:33] neg_lo:[0,1] neg_hi:[0,1]
	v_lshlrev_b32_e32 v38, 16, v17
	v_and_b32_e32 v39, 0xffff0000, v17
	v_pk_add_f32 v[32:33], v[32:33], v[38:39]
	v_lshlrev_b32_e32 v40, 16, v18
	v_pk_fma_f32 v[38:39], v[24:25], v[32:33], v[38:39] op_sel_hi:[0,1,1] neg_lo:[0,0,1] neg_hi:[0,0,1]
	v_cvt_pk_bf16_f32 v17, v38, v39
	v_lshlrev_b32_e32 v38, 16, v34
	v_and_b32_e32 v39, 0xffff0000, v34
	v_pk_add_f32 v[38:39], v[46:47], v[38:39] neg_lo:[0,1] neg_hi:[0,1]
	v_and_b32_e32 v41, 0xffff0000, v18
	v_pk_add_f32 v[38:39], v[38:39], v[40:41]
	v_lshlrev_b32_e32 v34, 16, v35
	v_pk_fma_f32 v[40:41], v[24:25], v[38:39], v[40:41] op_sel_hi:[0,1,1] neg_lo:[0,0,1] neg_hi:[0,0,1]
	v_or_b32_e32 v25, 7, v203
	v_min_i32_e32 v25, s0, v25
	v_cvt_f32_i32_e32 v37, v25
	v_and_b32_e32 v35, 0xffff0000, v35
	v_pk_add_f32 v[34:35], v[42:43], v[34:35] neg_lo:[0,1] neg_hi:[0,1]
	v_cvt_pk_bf16_f32 v18, v40, v41
	v_div_scale_f32 v42, s[18:19], v37, v37, 1.0
	v_lshlrev_b32_e32 v40, 16, v19
	v_and_b32_e32 v41, 0xffff0000, v19
	v_rcp_f32_e32 v43, v42
	v_pk_add_f32 v[34:35], v[34:35], v[40:41]
	s_nop 0
	v_pk_fma_f32 v[24:25], v[24:25], v[34:35], v[40:41] op_sel_hi:[0,1,1] neg_lo:[0,0,1] neg_hi:[0,0,1]
	v_cvt_pk_bf16_f32 v19, v24, v25
	ds_write_b128 v130, v[16:19] offset:80
	v_fma_f32 v16, -v42, v43, 1.0
	v_fmac_f32_e32 v43, v16, v43
	v_div_scale_f32 v16, vcc, 1.0, v37, 1.0
	v_mul_f32_e32 v17, v16, v43
	v_fma_f32 v18, -v42, v17, v16
	v_fmac_f32_e32 v17, v18, v43
	v_fma_f32 v16, -v42, v17, v16
	v_lshlrev_b32_e32 v18, 16, v28
	v_and_b32_e32 v19, 0xffff0000, v28
	v_div_fmas_f32 v16, v16, v43, v17
	v_pk_add_f32 v[18:19], v[26:27], v[18:19] neg_lo:[0,1] neg_hi:[0,1]
	v_lshlrev_b32_e32 v24, 16, v12
	v_and_b32_e32 v25, 0xffff0000, v12
	v_div_fixup_f32 v16, v16, v37, 1.0
	v_pk_add_f32 v[18:19], v[18:19], v[24:25]
	v_lshlrev_b32_e32 v26, 16, v13
	v_pk_fma_f32 v[24:25], v[16:17], v[18:19], v[24:25] op_sel_hi:[0,1,1] neg_lo:[0,0,1] neg_hi:[0,0,1]
	v_cvt_pk_bf16_f32 v12, v24, v25
	v_lshlrev_b32_e32 v24, 16, v29
	v_and_b32_e32 v25, 0xffff0000, v29
	v_pk_add_f32 v[24:25], v[32:33], v[24:25] neg_lo:[0,1] neg_hi:[0,1]
	v_and_b32_e32 v27, 0xffff0000, v13
	v_pk_add_f32 v[24:25], v[24:25], v[26:27]
	v_lshlrev_b32_e32 v28, 16, v14
	v_pk_fma_f32 v[26:27], v[16:17], v[24:25], v[26:27] op_sel_hi:[0,1,1] neg_lo:[0,0,1] neg_hi:[0,0,1]
	v_cvt_pk_bf16_f32 v13, v26, v27
	v_lshlrev_b32_e32 v26, 16, v30
	v_and_b32_e32 v27, 0xffff0000, v30
	v_pk_add_f32 v[26:27], v[38:39], v[26:27] neg_lo:[0,1] neg_hi:[0,1]
	v_and_b32_e32 v29, 0xffff0000, v14
	v_pk_add_f32 v[26:27], v[26:27], v[28:29]
	v_lshlrev_b32_e32 v30, 16, v15
	v_pk_fma_f32 v[28:29], v[16:17], v[26:27], v[28:29] op_sel_hi:[0,1,1] neg_lo:[0,0,1] neg_hi:[0,0,1]
	v_add_u32_e32 v17, 8, v203
	v_min_i32_e32 v17, s0, v17
	v_cvt_f32_i32_e32 v32, v17
	v_cvt_pk_bf16_f32 v14, v28, v29
	v_lshlrev_b32_e32 v28, 16, v31
	v_and_b32_e32 v29, 0xffff0000, v31
	v_div_scale_f32 v33, s[18:19], v32, v32, 1.0
	v_pk_add_f32 v[28:29], v[34:35], v[28:29] neg_lo:[0,1] neg_hi:[0,1]
	v_and_b32_e32 v31, 0xffff0000, v15
	v_rcp_f32_e32 v34, v33
	v_pk_add_f32 v[28:29], v[28:29], v[30:31]
	s_nop 0
	v_pk_fma_f32 v[16:17], v[16:17], v[28:29], v[30:31] op_sel_hi:[0,1,1] neg_lo:[0,0,1] neg_hi:[0,0,1]
	v_cvt_pk_bf16_f32 v15, v16, v17
	ds_write_b128 v130, v[12:15] offset:96
	v_fma_f32 v12, -v33, v34, 1.0
	v_fmac_f32_e32 v34, v12, v34
	v_div_scale_f32 v12, vcc, 1.0, v32, 1.0
	v_mul_f32_e32 v13, v12, v34
	v_fma_f32 v14, -v33, v13, v12
	v_fmac_f32_e32 v13, v14, v34
	v_fma_f32 v12, -v33, v13, v12
	v_lshlrev_b32_e32 v14, 16, v20
	v_and_b32_e32 v15, 0xffff0000, v20
	v_div_fmas_f32 v12, v12, v34, v13
	v_pk_add_f32 v[14:15], v[18:19], v[14:15] neg_lo:[0,1] neg_hi:[0,1]
	v_lshlrev_b32_e32 v16, 16, v8
	v_and_b32_e32 v17, 0xffff0000, v8
	v_div_fixup_f32 v12, v12, v32, 1.0
	v_pk_add_f32 v[14:15], v[14:15], v[16:17]
	s_nop 0
	v_pk_fma_f32 v[14:15], v[12:13], v[14:15], v[16:17] op_sel_hi:[0,1,1] neg_lo:[0,0,1] neg_hi:[0,0,1]
	v_cvt_pk_bf16_f32 v8, v14, v15
	v_lshlrev_b32_e32 v14, 16, v21
	v_and_b32_e32 v15, 0xffff0000, v21
	v_pk_add_f32 v[14:15], v[24:25], v[14:15] neg_lo:[0,1] neg_hi:[0,1]
	v_lshlrev_b32_e32 v16, 16, v9
	v_and_b32_e32 v17, 0xffff0000, v9
	v_pk_add_f32 v[14:15], v[14:15], v[16:17]
	s_nop 0
	v_pk_fma_f32 v[14:15], v[12:13], v[14:15], v[16:17] op_sel_hi:[0,1,1] neg_lo:[0,0,1] neg_hi:[0,0,1]
	v_cvt_pk_bf16_f32 v9, v14, v15
	v_lshlrev_b32_e32 v14, 16, v22
	v_and_b32_e32 v15, 0xffff0000, v22
	v_pk_add_f32 v[14:15], v[26:27], v[14:15] neg_lo:[0,1] neg_hi:[0,1]
	v_lshlrev_b32_e32 v16, 16, v10
	v_and_b32_e32 v17, 0xffff0000, v10
	v_pk_add_f32 v[14:15], v[14:15], v[16:17]
	s_nop 0
	v_pk_fma_f32 v[14:15], v[12:13], v[14:15], v[16:17] op_sel_hi:[0,1,1] neg_lo:[0,0,1] neg_hi:[0,0,1]
	v_cvt_pk_bf16_f32 v10, v14, v15
	v_lshlrev_b32_e32 v14, 16, v23
	v_and_b32_e32 v15, 0xffff0000, v23
	v_pk_add_f32 v[14:15], v[28:29], v[14:15] neg_lo:[0,1] neg_hi:[0,1]
	v_lshlrev_b32_e32 v16, 16, v11
	v_and_b32_e32 v17, 0xffff0000, v11
	v_pk_add_f32 v[14:15], v[14:15], v[16:17]
	s_nop 0
	v_pk_fma_f32 v[12:13], v[12:13], v[14:15], v[16:17] op_sel_hi:[0,1,1] neg_lo:[0,0,1] neg_hi:[0,0,1]
	v_cvt_pk_bf16_f32 v11, v12, v13
	v_mov_b32_e32 v12, 0x70
	v_lshl_or_b32 v12, v189, 4, v12
	v_add_u32_e32 v12, v36, v12
	ds_write_b128 v12, v[8:11]
	v_lshlrev_b32_e32 v8, 11, v202
	s_waitcnt vmcnt(0) lgkmcnt(0)
	s_barrier
; #define LAS __attribute__((address_space(3)))
; #define MFMA32(a, b, c) __builtin_amdgcn_mfma_f32_32x32x16_bf16((a), (b), (c), 0, 0, 0)
; __device__ __forceinline__ void pool_unit(LAS unsigned char* lds, const bf16* proj, const bf16* poolT, const float* pscale, bf16* Y, int tb, int g, int tid, int lane, int wid, Stopwatch& sw) {
;     ...
;     f32x16 acc[4];
; #pragma unroll
;     for (int k = 0; k < 4; ++k) acc[k] = splat16(0.f);
; #pragma unroll
;     for (int s = 0; s < 16; ++s)
; #pragma unroll
;         for (int k = 0; k < 4; ++k) { const bf16x8 a = *(const LAS bf16x8*)(lds + (2 * s + hi) * 2048 + (32 * k + r32) * 16); acc[k] = MFMA32(a, bfr[s], acc[k]); }
	v_add3_u32 v136, 0, v8, v188
	ds_read_b128 v[8:11], v136
	ds_read_b128 v[12:15], v136 offset:512
	s_waitcnt lgkmcnt(0)
	v_mfma_f32_32x32x16_bf16 v[52:67], v[8:11], v[4:7], 0
	v_mfma_f32_32x32x16_bf16 v[36:51], v[12:15], v[4:7], 0
	ds_read_b128 v[8:11], v136 offset:1024
	ds_read_b128 v[12:15], v136 offset:1536
	ds_read_b128 v[128:131], v136 offset:4096
	ds_read_b128 v[132:135], v136 offset:4608
	s_waitcnt lgkmcnt(3)
	v_mfma_f32_32x32x16_bf16 v[20:35], v[8:11], v[4:7], 0
	s_waitcnt lgkmcnt(2)
	v_mfma_f32_32x32x16_bf16 v[4:19], v[12:15], v[4:7], 0
	s_waitcnt lgkmcnt(1)
	v_mfma_f32_32x32x16_bf16 v[52:67], v[128:131], v[124:127], v[52:67]
	s_waitcnt lgkmcnt(0)
	v_mfma_f32_32x32x16_bf16 v[36:51], v[132:135], v[124:127], v[36:51]
	ds_read_b128 v[128:131], v136 offset:5120
	ds_read_b128 v[132:135], v136 offset:5632
	s_waitcnt lgkmcnt(1)
	v_mfma_f32_32x32x16_bf16 v[20:35], v[128:131], v[124:127], v[20:35]
	s_waitcnt lgkmcnt(0)
	v_mfma_f32_32x32x16_bf16 v[4:19], v[132:135], v[124:127], v[4:19]
	ds_read_b128 v[124:127], v136 offset:8192
	ds_read_b128 v[128:131], v136 offset:8704
	s_waitcnt lgkmcnt(1)
	v_mfma_f32_32x32x16_bf16 v[52:67], v[124:127], v[120:123], v[52:67]
	s_waitcnt lgkmcnt(0)
	v_mfma_f32_32x32x16_bf16 v[36:51], v[128:131], v[120:123], v[36:51]
	ds_read_b128 v[124:127], v136 offset:9216
	ds_read_b128 v[128:131], v136 offset:9728
	s_waitcnt lgkmcnt(1)
	v_mfma_f32_32x32x16_bf16 v[20:35], v[124:127], v[120:123], v[20:35]
	s_waitcnt lgkmcnt(0)
	v_mfma_f32_32x32x16_bf16 v[4:19], v[128:131], v[120:123], v[4:19]
	ds_read_b128 v[120:123], v136 offset:12288
	ds_read_b128 v[124:127], v136 offset:12800
	s_waitcnt lgkmcnt(1)
	v_mfma_f32_32x32x16_bf16 v[52:67], v[120:123], v[116:119], v[52:67]
	s_waitcnt lgkmcnt(0)
	v_mfma_f32_32x32x16_bf16 v[36:51], v[124:127], v[116:119], v[36:51]
	ds_read_b128 v[120:123], v136 offset:13312
	ds_read_b128 v[124:127], v136 offset:13824
	s_waitcnt lgkmcnt(1)
	v_mfma_f32_32x32x16_bf16 v[20:35], v[120:123], v[116:119], v[20:35]
	s_waitcnt lgkmcnt(0)
	v_mfma_f32_32x32x16_bf16 v[4:19], v[124:127], v[116:119], v[4:19]
	ds_read_b128 v[116:119], v136 offset:16384
	ds_read_b128 v[120:123], v136 offset:16896
	s_waitcnt lgkmcnt(1)
	v_mfma_f32_32x32x16_bf16 v[52:67], v[116:119], v[112:115], v[52:67]
	s_waitcnt lgkmcnt(0)
	v_mfma_f32_32x32x16_bf16 v[36:51], v[120:123], v[112:115], v[36:51]
	ds_read_b128 v[116:119], v136 offset:17408
	ds_read_b128 v[120:123], v136 offset:17920
	s_waitcnt lgkmcnt(1)
	v_mfma_f32_32x32x16_bf16 v[20:35], v[116:119], v[112:115], v[20:35]
	s_waitcnt lgkmcnt(0)
	v_mfma_f32_32x32x16_bf16 v[4:19], v[120:123], v[112:115], v[4:19]
	ds_read_b128 v[112:115], v136 offset:20480
	ds_read_b128 v[116:119], v136 offset:20992
	s_waitcnt lgkmcnt(1)
	v_mfma_f32_32x32x16_bf16 v[52:67], v[112:115], v[108:111], v[52:67]
	s_waitcnt lgkmcnt(0)
	v_mfma_f32_32x32x16_bf16 v[36:51], v[116:119], v[108:111], v[36:51]
	ds_read_b128 v[112:115], v136 offset:21504
	ds_read_b128 v[116:119], v136 offset:22016
	s_waitcnt lgkmcnt(1)
	v_mfma_f32_32x32x16_bf16 v[20:35], v[112:115], v[108:111], v[20:35]
	s_waitcnt lgkmcnt(0)
	v_mfma_f32_32x32x16_bf16 v[4:19], v[116:119], v[108:111], v[4:19]
	ds_read_b128 v[108:111], v136 offset:24576
	ds_read_b128 v[112:115], v136 offset:25088
	s_waitcnt lgkmcnt(1)
	v_mfma_f32_32x32x16_bf16 v[52:67], v[108:111], v[104:107], v[52:67]
	s_waitcnt lgkmcnt(0)
	v_mfma_f32_32x32x16_bf16 v[36:51], v[112:115], v[104:107], v[36:51]
	ds_read_b128 v[108:111], v136 offset:25600
	ds_read_b128 v[112:115], v136 offset:26112
	s_waitcnt lgkmcnt(1)
	v_mfma_f32_32x32x16_bf16 v[20:35], v[108:111], v[104:107], v[20:35]
	s_waitcnt lgkmcnt(0)
	v_mfma_f32_32x32x16_bf16 v[4:19], v[112:115], v[104:107], v[4:19]
	ds_read_b128 v[104:107], v136 offset:28672
	ds_read_b128 v[108:111], v136 offset:29184
	s_waitcnt lgkmcnt(1)
	v_mfma_f32_32x32x16_bf16 v[52:67], v[104:107], v[100:103], v[52:67]
	s_waitcnt lgkmcnt(0)
	v_mfma_f32_32x32x16_bf16 v[36:51], v[108:111], v[100:103], v[36:51]
	ds_read_b128 v[104:107], v136 offset:29696
	ds_read_b128 v[108:111], v136 offset:30208
	s_waitcnt lgkmcnt(1)
	v_mfma_f32_32x32x16_bf16 v[20:35], v[104:107], v[100:103], v[20:35]
	s_waitcnt lgkmcnt(0)
	v_mfma_f32_32x32x16_bf16 v[4:19], v[108:111], v[100:103], v[4:19]
	ds_read_b128 v[100:103], v136 offset:32768
	ds_read_b128 v[104:107], v136 offset:33280
	s_waitcnt lgkmcnt(1)
	v_mfma_f32_32x32x16_bf16 v[52:67], v[100:103], v[96:99], v[52:67]
	s_waitcnt lgkmcnt(0)
	v_mfma_f32_32x32x16_bf16 v[36:51], v[104:107], v[96:99], v[36:51]
	ds_read_b128 v[100:103], v136 offset:33792
	ds_read_b128 v[104:107], v136 offset:34304
	s_waitcnt lgkmcnt(1)
	v_mfma_f32_32x32x16_bf16 v[20:35], v[100:103], v[96:99], v[20:35]
	s_waitcnt lgkmcnt(0)
	v_mfma_f32_32x32x16_bf16 v[4:19], v[104:107], v[96:99], v[4:19]
	ds_read_b128 v[96:99], v136 offset:36864
	ds_read_b128 v[100:103], v136 offset:37376
	s_waitcnt lgkmcnt(1)
	v_mfma_f32_32x32x16_bf16 v[52:67], v[96:99], v[92:95], v[52:67]
	s_waitcnt lgkmcnt(0)
	v_mfma_f32_32x32x16_bf16 v[36:51], v[100:103], v[92:95], v[36:51]
	ds_read_b128 v[96:99], v136 offset:37888
	ds_read_b128 v[100:103], v136 offset:38400
	s_waitcnt lgkmcnt(1)
	v_mfma_f32_32x32x16_bf16 v[20:35], v[96:99], v[92:95], v[20:35]
	s_waitcnt lgkmcnt(0)
	v_mfma_f32_32x32x16_bf16 v[4:19], v[100:103], v[92:95], v[4:19]
	ds_read_b128 v[92:95], v136 offset:40960
	ds_read_b128 v[96:99], v136 offset:41472
	s_waitcnt lgkmcnt(1)
	v_mfma_f32_32x32x16_bf16 v[52:67], v[92:95], v[88:91], v[52:67]
	s_waitcnt lgkmcnt(0)
	v_mfma_f32_32x32x16_bf16 v[36:51], v[96:99], v[88:91], v[36:51]
	ds_read_b128 v[92:95], v136 offset:41984
	ds_read_b128 v[96:99], v136 offset:42496
	s_waitcnt lgkmcnt(1)
; #define TS_BEG(sw, id) do { if ((id) == TSSEL && (sw).on) (sw).t0 = __builtin_amdgcn_s_memrealtime(); } while (0)
; #define TS_END(sw, id) do { if ((id) == TSSEL && (sw).on) (sw).acc += __builtin_amdgcn_s_memrealtime() - (sw).t0; } while (0)
; #define TS_BEG(sw, id) do { } while (0)
; #define TS_END(sw, id) do { } while (0)
; #define LAS __attribute__((address_space(3)))
; __device__ __forceinline__ unsigned pk2(float lo, float hi) { f32x2_t_ v = {lo, hi}; bf16x2_t_ b = __builtin_convertvector(v, bf16x2_t_); return __builtin_bit_cast(unsigned, b); }
; __device__ __forceinline__ int crow(int r, int hi) { return (r & 3) + 8 * (r >> 2) + 4 * hi; }
; #define MFMA32(a, b, c) __builtin_amdgcn_mfma_f32_32x32x16_bf16((a), (b), (c), 0, 0, 0)
; __device__ __forceinline__ void pool_unit(LAS unsigned char* lds, const bf16* proj, const bf16* poolT, const float* pscale, bf16* Y, int tb, int g, int tid, int lane, int wid, Stopwatch& sw) {
;     ...
;     for (int s = 0; s < 16; ++s)
; #pragma unroll
;         for (int k = 0; k < 4; ++k) { const bf16x8 a = *(const LAS bf16x8*)(lds + (2 * s + hi) * 2048 + (32 * k + r32) * 16); acc[k] = MFMA32(a, bfr[s], acc[k]); }
;     TS_END(sw, 77); TS_BEG(sw, 78);
;     const int oc = g * 256 + 32 * wid + r32; const float ps = pscale[oc];
; #pragma unroll
;     for (int k = 0; k < 4; ++k)
; #pragma unroll
;         for (int r = 0; r < 16; ++r) { const int tok = 32 * k + crow(r, hi); Y[(size_t)(t0 + tok) * LDY + oc] = (bf16)(pk2(acc[k][r] * ps, 0.f) & 0xffffu); }
	v_mfma_f32_32x32x16_bf16 v[20:35], v[92:95], v[88:91], v[20:35]
	s_waitcnt lgkmcnt(0)
	v_mfma_f32_32x32x16_bf16 v[4:19], v[96:99], v[88:91], v[4:19]
	ds_read_b128 v[88:91], v136 offset:45056
	ds_read_b128 v[92:95], v136 offset:45568
	s_waitcnt lgkmcnt(1)
	v_mfma_f32_32x32x16_bf16 v[52:67], v[88:91], v[84:87], v[52:67]
	s_waitcnt lgkmcnt(0)
	v_mfma_f32_32x32x16_bf16 v[36:51], v[92:95], v[84:87], v[36:51]
	ds_read_b128 v[88:91], v136 offset:46080
	ds_read_b128 v[92:95], v136 offset:46592
	s_waitcnt lgkmcnt(1)
	v_mfma_f32_32x32x16_bf16 v[20:35], v[88:91], v[84:87], v[20:35]
	s_waitcnt lgkmcnt(0)
	v_mfma_f32_32x32x16_bf16 v[4:19], v[92:95], v[84:87], v[4:19]
	ds_read_b128 v[84:87], v136 offset:49152
	ds_read_b128 v[88:91], v136 offset:49664
	s_waitcnt lgkmcnt(1)
	v_mfma_f32_32x32x16_bf16 v[52:67], v[84:87], v[80:83], v[52:67]
	s_waitcnt lgkmcnt(0)
	v_mfma_f32_32x32x16_bf16 v[36:51], v[88:91], v[80:83], v[36:51]
	ds_read_b128 v[84:87], v136 offset:50176
	ds_read_b128 v[88:91], v136 offset:50688
	s_waitcnt lgkmcnt(1)
	v_mfma_f32_32x32x16_bf16 v[20:35], v[84:87], v[80:83], v[20:35]
	s_waitcnt lgkmcnt(0)
	v_mfma_f32_32x32x16_bf16 v[4:19], v[88:91], v[80:83], v[4:19]
	ds_read_b128 v[80:83], v136 offset:53248
	ds_read_b128 v[84:87], v136 offset:53760
	s_waitcnt lgkmcnt(1)
	v_mfma_f32_32x32x16_bf16 v[52:67], v[80:83], v[76:79], v[52:67]
	s_waitcnt lgkmcnt(0)
	v_mfma_f32_32x32x16_bf16 v[36:51], v[84:87], v[76:79], v[36:51]
	ds_read_b128 v[80:83], v136 offset:54272
	ds_read_b128 v[84:87], v136 offset:54784
	s_waitcnt lgkmcnt(1)
	v_mfma_f32_32x32x16_bf16 v[20:35], v[80:83], v[76:79], v[20:35]
	s_waitcnt lgkmcnt(0)
	v_mfma_f32_32x32x16_bf16 v[4:19], v[84:87], v[76:79], v[4:19]
	ds_read_b128 v[76:79], v136 offset:57344
	ds_read_b128 v[80:83], v136 offset:57856
	s_waitcnt lgkmcnt(1)
	v_mfma_f32_32x32x16_bf16 v[52:67], v[76:79], v[72:75], v[52:67]
	s_waitcnt lgkmcnt(0)
	v_mfma_f32_32x32x16_bf16 v[36:51], v[80:83], v[72:75], v[36:51]
	ds_read_b128 v[76:79], v136 offset:58368
	ds_read_b128 v[80:83], v136 offset:58880
	s_waitcnt lgkmcnt(1)
	v_mfma_f32_32x32x16_bf16 v[20:35], v[76:79], v[72:75], v[20:35]
	s_waitcnt lgkmcnt(0)
	v_mfma_f32_32x32x16_bf16 v[4:19], v[80:83], v[72:75], v[4:19]
	ds_read_b128 v[72:75], v136 offset:61440
	ds_read_b128 v[76:79], v136 offset:61952
	v_lshl_add_u64 v[80:81], v[2:3], 2, s[38:39]
	s_waitcnt lgkmcnt(1)
	v_mfma_f32_32x32x16_bf16 v[52:67], v[72:75], v[68:71], v[52:67]
	ds_read_b128 v[72:75], v136 offset:62464
	s_waitcnt lgkmcnt(1)
	v_mfma_f32_32x32x16_bf16 v[36:51], v[76:79], v[68:71], v[36:51]
	ds_read_b128 v[76:79], v136 offset:62976
	s_waitcnt lgkmcnt(1)
	v_mfma_f32_32x32x16_bf16 v[20:35], v[72:75], v[68:71], v[20:35]
	global_load_dword v72, v[80:81], off
	v_lshl_or_b32 v73, v202, 2, s4
	v_readlane_b32 s4, v253, 61
	v_readlane_b32 s5, v253, 62
	s_waitcnt vmcnt(0)
	s_nop 3
	v_mul_f32_e32 v36, v36, v72
	s_waitcnt lgkmcnt(0)
	v_mfma_f32_32x32x16_bf16 v[4:19], v[76:79], v[68:71], v[4:19]
	v_lshl_add_u64 v[68:69], v[2:3], 1, s[4:5]
	v_mul_f32_e32 v2, v52, v72
	v_cvt_pk_bf16_f32 v2, v2, s0
	v_mad_i64_i32 v[70:71], s[4:5], v73, s67, v[68:69]
	global_store_short v[70:71], v2, off
	v_mul_f32_e32 v2, v53, v72
	v_or_b32_e32 v52, 1, v73
	v_cvt_pk_bf16_f32 v2, v2, s0
	v_mad_i64_i32 v[52:53], s[4:5], v52, s67, v[68:69]
	global_store_short v[52:53], v2, off
	v_mul_f32_e32 v2, v54, v72
	v_or_b32_e32 v52, 2, v73
	v_cvt_pk_bf16_f32 v2, v2, s0
	v_mad_i64_i32 v[52:53], s[4:5], v52, s67, v[68:69]
	global_store_short v[52:53], v2, off
	v_mul_f32_e32 v2, v55, v72
	v_or_b32_e32 v52, 3, v73
	v_cvt_pk_bf16_f32 v2, v2, s0
	v_mad_i64_i32 v[52:53], s[4:5], v52, s67, v[68:69]
	global_store_short v[52:53], v2, off
	v_mul_f32_e32 v2, v56, v72
	v_or_b32_e32 v52, 8, v73
	v_cvt_pk_bf16_f32 v2, v2, s0
	v_mad_i64_i32 v[52:53], s[4:5], v52, s67, v[68:69]
	global_store_short v[52:53], v2, off
	v_mul_f32_e32 v2, v57, v72
	v_or_b32_e32 v52, 9, v73
	v_cvt_pk_bf16_f32 v2, v2, s0
	v_mad_i64_i32 v[52:53], s[4:5], v52, s67, v[68:69]
	global_store_short v[52:53], v2, off
	v_mul_f32_e32 v2, v58, v72
	v_or_b32_e32 v52, 10, v73
	v_cvt_pk_bf16_f32 v2, v2, s0
	v_mad_i64_i32 v[52:53], s[4:5], v52, s67, v[68:69]
	global_store_short v[52:53], v2, off
	v_mul_f32_e32 v2, v59, v72
	v_or_b32_e32 v52, 11, v73
	v_cvt_pk_bf16_f32 v2, v2, s0
	v_mad_i64_i32 v[52:53], s[4:5], v52, s67, v[68:69]
	global_store_short v[52:53], v2, off
	v_mul_f32_e32 v2, v60, v72
	v_or_b32_e32 v52, 16, v73
	v_cvt_pk_bf16_f32 v2, v2, s0
	v_mad_i64_i32 v[52:53], s[4:5], v52, s67, v[68:69]
	global_store_short v[52:53], v2, off
	v_mul_f32_e32 v2, v61, v72
	v_or_b32_e32 v52, 17, v73
	v_cvt_pk_bf16_f32 v2, v2, s0
	v_mad_i64_i32 v[52:53], s[4:5], v52, s67, v[68:69]
	global_store_short v[52:53], v2, off
	v_mul_f32_e32 v2, v62, v72
	v_or_b32_e32 v52, 18, v73
	v_cvt_pk_bf16_f32 v2, v2, s0
	v_mad_i64_i32 v[52:53], s[4:5], v52, s67, v[68:69]
	global_store_short v[52:53], v2, off
	v_mul_f32_e32 v2, v63, v72
	v_or_b32_e32 v52, 19, v73
	v_cvt_pk_bf16_f32 v2, v2, s0
	v_mad_i64_i32 v[52:53], s[4:5], v52, s67, v[68:69]
	global_store_short v[52:53], v2, off
	v_mul_f32_e32 v2, v64, v72
	v_or_b32_e32 v52, 24, v73
	v_cvt_pk_bf16_f32 v2, v2, s0
	v_mad_i64_i32 v[52:53], s[4:5], v52, s67, v[68:69]
	global_store_short v[52:53], v2, off
	v_mul_f32_e32 v2, v65, v72
	v_or_b32_e32 v52, 25, v73
	v_cvt_pk_bf16_f32 v2, v2, s0
	v_mad_i64_i32 v[52:53], s[4:5], v52, s67, v[68:69]
	global_store_short v[52:53], v2, off
	v_mul_f32_e32 v2, v66, v72
	v_or_b32_e32 v52, 26, v73
	v_cvt_pk_bf16_f32 v2, v2, s0
	v_mad_i64_i32 v[52:53], s[4:5], v52, s67, v[68:69]
	global_store_short v[52:53], v2, off
	v_mul_f32_e32 v2, v67, v72
	v_or_b32_e32 v52, 27, v73
; __device__ __forceinline__ unsigned pk2(float lo, float hi) { f32x2_t_ v = {lo, hi}; bf16x2_t_ b = __builtin_convertvector(v, bf16x2_t_); return __builtin_bit_cast(unsigned, b); }
; __device__ __forceinline__ int crow(int r, int hi) { return (r & 3) + 8 * (r >> 2) + 4 * hi; }
; __device__ __forceinline__ void pool_unit(LAS unsigned char* lds, const bf16* proj, const bf16* poolT, const float* pscale, bf16* Y, int tb, int g, int tid, int lane, int wid, Stopwatch& sw) {
;     ...
;     const int oc = g * 256 + 32 * wid + r32; const float ps = pscale[oc];
; #pragma unroll
;     for (int k = 0; k < 4; ++k)
; #pragma unroll
;         for (int r = 0; r < 16; ++r) { const int tok = 32 * k + crow(r, hi); Y[(size_t)(t0 + tok) * LDY + oc] = (bf16)(pk2(acc[k][r] * ps, 0.f) & 0xffffu); }
	v_cvt_pk_bf16_f32 v2, v2, s0
	v_mad_i64_i32 v[52:53], s[4:5], v52, s67, v[68:69]
	global_store_short v[52:53], v2, off
	v_or_b32_e32 v2, 32, v73
	v_cvt_pk_bf16_f32 v36, v36, s0
	v_mad_i64_i32 v[52:53], s[4:5], v2, s67, v[68:69]
	global_store_short v[52:53], v36, off
	v_mul_f32_e32 v2, v37, v72
	v_or_b32_e32 v36, 33, v73
	v_cvt_pk_bf16_f32 v2, v2, s0
	v_mad_i64_i32 v[36:37], s[4:5], v36, s67, v[68:69]
	global_store_short v[36:37], v2, off
	v_mul_f32_e32 v2, v38, v72
	v_or_b32_e32 v36, 34, v73
	v_cvt_pk_bf16_f32 v2, v2, s0
	v_mad_i64_i32 v[36:37], s[4:5], v36, s67, v[68:69]
	global_store_short v[36:37], v2, off
	v_mul_f32_e32 v2, v39, v72
	v_or_b32_e32 v36, 35, v73
	v_cvt_pk_bf16_f32 v2, v2, s0
	v_mad_i64_i32 v[36:37], s[4:5], v36, s67, v[68:69]
	global_store_short v[36:37], v2, off
	v_mul_f32_e32 v2, v40, v72
	v_or_b32_e32 v36, 40, v73
	v_cvt_pk_bf16_f32 v2, v2, s0
	v_mad_i64_i32 v[36:37], s[4:5], v36, s67, v[68:69]
	global_store_short v[36:37], v2, off
	v_mul_f32_e32 v2, v41, v72
	v_or_b32_e32 v36, 41, v73
	v_cvt_pk_bf16_f32 v2, v2, s0
	v_mad_i64_i32 v[36:37], s[4:5], v36, s67, v[68:69]
	global_store_short v[36:37], v2, off
	v_mul_f32_e32 v2, v42, v72
	v_or_b32_e32 v36, 42, v73
	v_cvt_pk_bf16_f32 v2, v2, s0
	v_mad_i64_i32 v[36:37], s[4:5], v36, s67, v[68:69]
	global_store_short v[36:37], v2, off
	v_mul_f32_e32 v2, v43, v72
	v_or_b32_e32 v36, 43, v73
	v_cvt_pk_bf16_f32 v2, v2, s0
	v_mad_i64_i32 v[36:37], s[4:5], v36, s67, v[68:69]
	global_store_short v[36:37], v2, off
	v_mul_f32_e32 v2, v44, v72
	v_or_b32_e32 v36, 48, v73
	v_cvt_pk_bf16_f32 v2, v2, s0
	v_mad_i64_i32 v[36:37], s[4:5], v36, s67, v[68:69]
	global_store_short v[36:37], v2, off
	v_mul_f32_e32 v2, v45, v72
	v_or_b32_e32 v36, 49, v73
	v_cvt_pk_bf16_f32 v2, v2, s0
	v_mad_i64_i32 v[36:37], s[4:5], v36, s67, v[68:69]
	global_store_short v[36:37], v2, off
	v_mul_f32_e32 v2, v46, v72
	v_or_b32_e32 v36, 50, v73
	v_cvt_pk_bf16_f32 v2, v2, s0
	v_mad_i64_i32 v[36:37], s[4:5], v36, s67, v[68:69]
	global_store_short v[36:37], v2, off
	v_mul_f32_e32 v2, v47, v72
	v_or_b32_e32 v36, 51, v73
	v_cvt_pk_bf16_f32 v2, v2, s0
	v_mad_i64_i32 v[36:37], s[4:5], v36, s67, v[68:69]
	global_store_short v[36:37], v2, off
	v_mul_f32_e32 v2, v48, v72
	v_or_b32_e32 v36, 56, v73
	v_cvt_pk_bf16_f32 v2, v2, s0
	v_mad_i64_i32 v[36:37], s[4:5], v36, s67, v[68:69]
	global_store_short v[36:37], v2, off
	v_mul_f32_e32 v2, v49, v72
	v_or_b32_e32 v36, 57, v73
	v_cvt_pk_bf16_f32 v2, v2, s0
	v_mad_i64_i32 v[36:37], s[4:5], v36, s67, v[68:69]
	global_store_short v[36:37], v2, off
	v_mul_f32_e32 v2, v50, v72
	v_or_b32_e32 v36, 58, v73
	v_cvt_pk_bf16_f32 v2, v2, s0
	v_mad_i64_i32 v[36:37], s[4:5], v36, s67, v[68:69]
	global_store_short v[36:37], v2, off
	v_mul_f32_e32 v2, v51, v72
	v_or_b32_e32 v36, 59, v73
	v_cvt_pk_bf16_f32 v2, v2, s0
	v_mad_i64_i32 v[36:37], s[4:5], v36, s67, v[68:69]
	global_store_short v[36:37], v2, off
	v_or_b32_e32 v2, 64, v73
	v_mul_f32_e32 v20, v20, v72
	v_cvt_pk_bf16_f32 v20, v20, s0
	v_mad_i64_i32 v[36:37], s[4:5], v2, s67, v[68:69]
	global_store_short v[36:37], v20, off
	v_mul_f32_e32 v2, v21, v72
	v_or_b32_e32 v20, 0x41, v73
	v_cvt_pk_bf16_f32 v2, v2, s0
	v_mad_i64_i32 v[20:21], s[4:5], v20, s67, v[68:69]
	global_store_short v[20:21], v2, off
	v_mul_f32_e32 v2, v22, v72
	v_or_b32_e32 v20, 0x42, v73
	v_cvt_pk_bf16_f32 v2, v2, s0
	v_mad_i64_i32 v[20:21], s[4:5], v20, s67, v[68:69]
	global_store_short v[20:21], v2, off
	v_mul_f32_e32 v2, v23, v72
	v_or_b32_e32 v20, 0x43, v73
	v_cvt_pk_bf16_f32 v2, v2, s0
	v_mad_i64_i32 v[20:21], s[4:5], v20, s67, v[68:69]
	global_store_short v[20:21], v2, off
	v_mul_f32_e32 v2, v24, v72
	v_or_b32_e32 v20, 0x48, v73
	v_cvt_pk_bf16_f32 v2, v2, s0
	v_mad_i64_i32 v[20:21], s[4:5], v20, s67, v[68:69]
	global_store_short v[20:21], v2, off
	v_mul_f32_e32 v2, v25, v72
	v_or_b32_e32 v20, 0x49, v73
	v_cvt_pk_bf16_f32 v2, v2, s0
	v_mad_i64_i32 v[20:21], s[4:5], v20, s67, v[68:69]
	global_store_short v[20:21], v2, off
	v_mul_f32_e32 v2, v26, v72
	v_or_b32_e32 v20, 0x4a, v73
	v_cvt_pk_bf16_f32 v2, v2, s0
	v_mad_i64_i32 v[20:21], s[4:5], v20, s67, v[68:69]
	global_store_short v[20:21], v2, off
	v_mul_f32_e32 v2, v27, v72
	v_or_b32_e32 v20, 0x4b, v73
	v_cvt_pk_bf16_f32 v2, v2, s0
	v_mad_i64_i32 v[20:21], s[4:5], v20, s67, v[68:69]
; #define WG_BAR() do { asm volatile("s_waitcnt vmcnt(0) lgkmcnt(0)" ::: "memory"); __builtin_amdgcn_s_barrier(); asm volatile("" ::: "memory"); } while (0)
; __device__ __forceinline__ unsigned pk2(float lo, float hi) { f32x2_t_ v = {lo, hi}; bf16x2_t_ b = __builtin_convertvector(v, bf16x2_t_); return __builtin_bit_cast(unsigned, b); }
; __device__ __forceinline__ int crow(int r, int hi) { return (r & 3) + 8 * (r >> 2) + 4 * hi; }
; __device__ __forceinline__ void pool_unit(LAS unsigned char* lds, const bf16* proj, const bf16* poolT, const float* pscale, bf16* Y, int tb, int g, int tid, int lane, int wid, Stopwatch& sw) {
;     ...
;     const int oc = g * 256 + 32 * wid + r32; const float ps = pscale[oc];
; #pragma unroll
;     for (int k = 0; k < 4; ++k)
; #pragma unroll
;         for (int r = 0; r < 16; ++r) { const int tok = 32 * k + crow(r, hi); Y[(size_t)(t0 + tok) * LDY + oc] = (bf16)(pk2(acc[k][r] * ps, 0.f) & 0xffffu); }
;     WG_BAR();
	global_store_short v[20:21], v2, off
	v_mul_f32_e32 v2, v28, v72
	v_or_b32_e32 v20, 0x50, v73
	v_cvt_pk_bf16_f32 v2, v2, s0
	v_mad_i64_i32 v[20:21], s[4:5], v20, s67, v[68:69]
	global_store_short v[20:21], v2, off
	v_mul_f32_e32 v2, v29, v72
	v_or_b32_e32 v20, 0x51, v73
	v_cvt_pk_bf16_f32 v2, v2, s0
	v_mad_i64_i32 v[20:21], s[4:5], v20, s67, v[68:69]
	global_store_short v[20:21], v2, off
	v_mul_f32_e32 v2, v30, v72
	v_or_b32_e32 v20, 0x52, v73
	v_cvt_pk_bf16_f32 v2, v2, s0
	v_mad_i64_i32 v[20:21], s[4:5], v20, s67, v[68:69]
	global_store_short v[20:21], v2, off
	v_mul_f32_e32 v2, v31, v72
	v_or_b32_e32 v20, 0x53, v73
	v_cvt_pk_bf16_f32 v2, v2, s0
	v_mad_i64_i32 v[20:21], s[4:5], v20, s67, v[68:69]
	global_store_short v[20:21], v2, off
	v_mul_f32_e32 v2, v32, v72
	v_or_b32_e32 v20, 0x58, v73
	v_cvt_pk_bf16_f32 v2, v2, s0
	v_mad_i64_i32 v[20:21], s[4:5], v20, s67, v[68:69]
	global_store_short v[20:21], v2, off
	v_mul_f32_e32 v2, v33, v72
	v_or_b32_e32 v20, 0x59, v73
	v_cvt_pk_bf16_f32 v2, v2, s0
	v_mad_i64_i32 v[20:21], s[4:5], v20, s67, v[68:69]
	global_store_short v[20:21], v2, off
	v_mul_f32_e32 v2, v34, v72
	v_or_b32_e32 v20, 0x5a, v73
	v_cvt_pk_bf16_f32 v2, v2, s0
	v_mad_i64_i32 v[20:21], s[4:5], v20, s67, v[68:69]
	global_store_short v[20:21], v2, off
	v_mul_f32_e32 v2, v35, v72
	v_or_b32_e32 v20, 0x5b, v73
	v_cvt_pk_bf16_f32 v2, v2, s0
	v_mad_i64_i32 v[20:21], s[4:5], v20, s67, v[68:69]
	global_store_short v[20:21], v2, off
	v_or_b32_e32 v2, 0x60, v73
	v_mul_f32_e32 v4, v72, v4
	v_cvt_pk_bf16_f32 v4, v4, s0
	v_mad_i64_i32 v[20:21], s[4:5], v2, s67, v[68:69]
	global_store_short v[20:21], v4, off
	v_mul_f32_e32 v2, v72, v5
	v_or_b32_e32 v4, 0x61, v73
	v_cvt_pk_bf16_f32 v2, v2, s0
	v_mad_i64_i32 v[4:5], s[4:5], v4, s67, v[68:69]
	global_store_short v[4:5], v2, off
	v_mul_f32_e32 v2, v72, v6
	v_or_b32_e32 v4, 0x62, v73
	v_cvt_pk_bf16_f32 v2, v2, s0
	v_mad_i64_i32 v[4:5], s[4:5], v4, s67, v[68:69]
	global_store_short v[4:5], v2, off
	v_mul_f32_e32 v2, v72, v7
	v_or_b32_e32 v4, 0x63, v73
	v_cvt_pk_bf16_f32 v2, v2, s0
	v_mad_i64_i32 v[4:5], s[4:5], v4, s67, v[68:69]
	global_store_short v[4:5], v2, off
	v_mul_f32_e32 v2, v72, v8
	v_or_b32_e32 v4, 0x68, v73
	v_cvt_pk_bf16_f32 v2, v2, s0
	v_mad_i64_i32 v[4:5], s[4:5], v4, s67, v[68:69]
	global_store_short v[4:5], v2, off
	v_mul_f32_e32 v2, v72, v9
	v_or_b32_e32 v4, 0x69, v73
	v_cvt_pk_bf16_f32 v2, v2, s0
	v_mad_i64_i32 v[4:5], s[4:5], v4, s67, v[68:69]
	global_store_short v[4:5], v2, off
	v_mul_f32_e32 v2, v72, v10
	v_or_b32_e32 v4, 0x6a, v73
	v_cvt_pk_bf16_f32 v2, v2, s0
	v_mad_i64_i32 v[4:5], s[4:5], v4, s67, v[68:69]
	global_store_short v[4:5], v2, off
	v_mul_f32_e32 v2, v72, v11
	v_or_b32_e32 v4, 0x6b, v73
	v_cvt_pk_bf16_f32 v2, v2, s0
	v_mad_i64_i32 v[4:5], s[4:5], v4, s67, v[68:69]
	global_store_short v[4:5], v2, off
	v_mul_f32_e32 v2, v72, v12
	v_or_b32_e32 v4, 0x70, v73
	v_cvt_pk_bf16_f32 v2, v2, s0
	v_mad_i64_i32 v[4:5], s[4:5], v4, s67, v[68:69]
	global_store_short v[4:5], v2, off
	v_mul_f32_e32 v2, v72, v13
	v_or_b32_e32 v4, 0x71, v73
	v_cvt_pk_bf16_f32 v2, v2, s0
	v_mad_i64_i32 v[4:5], s[4:5], v4, s67, v[68:69]
	global_store_short v[4:5], v2, off
	v_mul_f32_e32 v2, v72, v14
	v_or_b32_e32 v4, 0x72, v73
	v_cvt_pk_bf16_f32 v2, v2, s0
	v_mad_i64_i32 v[4:5], s[4:5], v4, s67, v[68:69]
	global_store_short v[4:5], v2, off
	v_mul_f32_e32 v2, v72, v15
	v_or_b32_e32 v4, 0x73, v73
	v_cvt_pk_bf16_f32 v2, v2, s0
	v_mad_i64_i32 v[4:5], s[4:5], v4, s67, v[68:69]
	global_store_short v[4:5], v2, off
	v_mul_f32_e32 v2, v72, v16
	v_or_b32_e32 v4, 0x78, v73
	v_cvt_pk_bf16_f32 v2, v2, s0
	v_mad_i64_i32 v[4:5], s[4:5], v4, s67, v[68:69]
	global_store_short v[4:5], v2, off
	v_mul_f32_e32 v2, v72, v17
	v_or_b32_e32 v4, 0x79, v73
	v_cvt_pk_bf16_f32 v2, v2, s0
	v_mad_i64_i32 v[4:5], s[4:5], v4, s67, v[68:69]
	global_store_short v[4:5], v2, off
	v_mul_f32_e32 v2, v72, v18
	v_or_b32_e32 v4, 0x7a, v73
	v_cvt_pk_bf16_f32 v2, v2, s0
	v_mad_i64_i32 v[4:5], s[4:5], v4, s67, v[68:69]
	global_store_short v[4:5], v2, off
	v_mul_f32_e32 v2, v72, v19
	v_or_b32_e32 v4, 0x7b, v73
	v_cvt_pk_bf16_f32 v2, v2, s0
	v_mad_i64_i32 v[4:5], s[4:5], v4, s67, v[68:69]
	global_store_short v[4:5], v2, off
	s_waitcnt vmcnt(0) lgkmcnt(0)
	s_barrier

; #define GAS __attribute__((address_space(1)))
; __device__ __forceinline__ void pool_unit(LAS unsigned char* lds, const bf16* proj, const bf16* poolT, const float* pscale, bf16* Y, int tb, int g, int tid, int lane, int wid, Stopwatch& sw) {
;     ...
;       { v4u pre[15];
; #pragma unroll
;         for (int j = 1; j < 16; ++j) { const v4u z0 = {0u, 0u, 0u, 0u}; pre[j - 1] = (j < win && pos0 - j >= 0) ? *(const GAS v4u*)(up + (long)(tsb * 8 - j) * LDP) : z0; }
; #pragma unroll
;         for (int j = 1; j < 16; ++j) { const v4u w = pre[j - 1];
;           aw[0] += bflo(w.x); aw[1] += bfhi(w.x); aw[2] += bflo(w.y); aw[3] += bfhi(w.y); aw[4] += bflo(w.z); aw[5] += bfhi(w.z); aw[6] += bflo(w.w); aw[7] += bfhi(w.w); } }
.LBB0_293:
	s_or_b64 exec, exec, s[44:45]
	v_cmp_lt_i32_e32 vcc, 4, v203
	s_xor_b64 s[42:43], s[42:43], -1
	s_and_b64 s[18:19], s[42:43], vcc
	v_mov_b32_e32 v128, 0
	v_mov_b32_e32 v132, 0
	v_mov_b32_e32 v133, 0
	v_mov_b32_e32 v134, 0
	v_mov_b32_e32 v135, 0
	s_and_saveexec_b64 s[44:45], s[18:19]
	s_cbranch_execz .LBB0_295
	v_add_u32_e32 v8, -5, v204
	v_mad_i64_i32 v[8:9], s[18:19], v8, s33, v[190:191]
	global_load_dwordx4 v[132:135], v[8:9], off
